# MLA tile loop: DMA source addresses kept in registers and advanced per tile instead of recomputed; max tree with v_max3
# baseline (speedup 1.0000x reference)
; template <int DQ>
; DI AtRd at_rd_init(int lane) {
;     AtRd r; const int kr = lane & 31, h = lane >> 5, i16 = lane & 15, q = i16 >> 2, pp = i16 & 3, blk = (lane >> 4) & 1;
;     const int f = at_kf<DQ>(kr);
;     r.kbase = kr * (DQ * 2) + ((f >> 3) << 7); r.kbase1 = kr * (DQ * 2) + (((f >> 3) ^ 1) << 7);
; #pragma unroll
;     for (int i = 0; i < 4; ++i) r.ko[i] = ((2 * i + h) ^ (f & 7)) << 4;
;     r.vbase = (4 * h + q) * 256 + 8 * pp;
; #pragma unroll
;     for (int t = 0; t < 4; ++t) r.vo[t] = ((2 * t + blk) ^ ((4 * h + q) & 7)) << 5;
;     return r;
; template <int DQ>
; DI AtDma at_dma_init(int ld_bytes, int wave, int lane) {
;     AtDma d; d.rope = 0u;
;     constexpr int PPR = DQ / 8;
; #pragma unroll
;     for (int k = 0; k < DQ / 64; ++k) { const int L = (wave + 8 * k) * 64 + lane, r = L / PPR, pc = (L % PPR) ^ at_kf<DQ>(r);
;         if (DQ == 192 && pc >= 16) { d.ko[k] = (unsigned)(r * 128 + (pc - 16) * 16); d.rope |= 1u << k; } else d.ko[k] = (unsigned)(r * ld_bytes + pc * 16); }
;     if (DQ == 128) d.ko[2] = 0u;
; #pragma unroll
;     for (int k = 0; k < 2; ++k) { const int L = (wave + 8 * k) * 64 + lane, r = L >> 4, pc = (L & 15) ^ (2 * (r & 7)); d.vo[k] = (unsigned)(r * ld_bytes + pc * 16); }
;     return d;
; }
.LBB0_530:
	s_cmp_gt_i32 s24, 5
	s_cselect_b64 s[0:1], -1, 0
	s_cmp_lt_i32 s25, 6
	s_cselect_b64 s[2:3], -1, 0
	s_or_b64 s[0:1], s[0:1], s[2:3]
	s_and_b64 vcc, exec, s[0:1]
	s_cbranch_vccnz .LBB0_622
	s_bitcmp1_b32 s26, 1
	s_cbranch_scc1 .LBB0_560
	v_readfirstlane_b32 s2, v0
	s_movk_i32 s0, 0xffc0
	s_nop 0
	v_mov_b32_e32 v1, s2
	v_bfi_b32 v2, s0, v1, v0
	s_mov_b32 s0, 0x2aaaaaab
	v_mul_hi_i32 v1, v2, s0
	v_lshrrev_b32_e32 v3, 31, v1
	v_ashrrev_i32_e32 v1, 2, v1
	v_add_u32_e32 v1, v1, v3
	v_mul_lo_u32 v3, v1, 24
	v_sub_u32_e32 v3, v2, v3
	v_lshrrev_b32_e32 v4, 1, v1
	v_bitop3_b32 v3, v4, v3, 7 bitop3:0x6c
	v_cmp_gt_i32_e32 vcc, 16, v3
	v_lshlrev_b32_e32 v3, 4, v3
	s_and_saveexec_b64 s[0:1], vcc
	s_xor_b64 s[0:1], exec, s[0:1]
	v_lshl_add_u32 v162, v1, 12, v3
	s_or_saveexec_b64 s[0:1], s[0:1]
	v_mov_b32_e32 v4, 0
	s_xor_b64 exec, exec, s[0:1]
	v_lshlrev_b32_e32 v1, 7, v1
	s_movk_i32 s3, 0xff00
	v_add3_u32 v162, v1, v3, s3
	v_mov_b32_e32 v4, 1
	s_or_b64 exec, exec, s[0:1]
	v_add_u32_e32 v5, 0x200, v2
	s_mov_b32 s0, 0x2aaaaaab
	v_mul_hi_i32 v1, v5, s0
	v_lshrrev_b32_e32 v3, 31, v1
	v_ashrrev_i32_e32 v1, 2, v1
	v_add_u32_e32 v1, v1, v3
	v_mul_lo_u32 v3, v1, 24
	v_sub_u32_e32 v3, v5, v3
	v_lshrrev_b32_e32 v6, 1, v1
	v_bitop3_b32 v3, v6, v3, 7 bitop3:0x6c
	v_cmp_gt_i32_e32 vcc, 16, v3
	v_lshlrev_b32_e32 v3, 4, v3
	s_and_saveexec_b64 s[0:1], vcc
	s_xor_b64 s[0:1], exec, s[0:1]
	v_lshl_add_u32 v164, v1, 12, v3
	s_andn2_saveexec_b64 s[0:1], s[0:1]
	v_lshlrev_b32_e32 v1, 7, v1
	s_movk_i32 s3, 0xff00
	v_add3_u32 v164, v1, v3, s3
	v_or_b32_e32 v4, 2, v4
	s_or_b64 exec, exec, s[0:1]
	v_add_u32_e32 v3, 0x400, v2
	s_mov_b32 s0, 0x2aaaaaab
	v_mul_hi_i32 v1, v3, s0
	v_lshrrev_b32_e32 v6, 31, v1
	v_ashrrev_i32_e32 v1, 2, v1
	v_add_u32_e32 v1, v1, v6
	v_mul_lo_u32 v6, v1, 24
	v_sub_u32_e32 v3, v3, v6
	v_lshrrev_b32_e32 v6, 1, v1
	v_bitop3_b32 v3, v6, v3, 7 bitop3:0x6c
	v_cmp_gt_i32_e32 vcc, 16, v3
	v_lshlrev_b32_e32 v6, 4, v3
	s_and_saveexec_b64 s[0:1], vcc
	s_xor_b64 s[0:1], exec, s[0:1]
	v_lshl_add_u32 v166, v1, 12, v6
	s_or_saveexec_b64 s[0:1], s[0:1]
	v_and_b32_e32 v3, 63, v0
	s_xor_b64 exec, exec, s[0:1]
	v_lshlrev_b32_e32 v1, 7, v1
	s_movk_i32 s3, 0xff00
	v_add3_u32 v166, v1, v6, s3
	v_or_b32_e32 v4, 4, v4
	s_or_b64 exec, exec, s[0:1]
	v_lshrrev_b32_e32 v6, 5, v3
	v_bfe_u32 v10, v0, 1, 3
	s_lshr_b32 s2, s2, 6
	v_bitop3_b32 v11, v6, v10, 2 bitop3:0x36
	s_add_u32 s0, s50, 0x2c5ae000
	v_lshrrev_b32_e32 v1, 1, v0
	v_lshlrev_b32_e32 v180, 4, v11
	v_bitop3_b32 v11, v6, v10, 4 bitop3:0x36
	v_bitop3_b32 v10, v6, v10, 6 bitop3:0x36
	s_addc_u32 s1, s51, 0
	v_bitop3_b32 v1, v6, v1, 7 bitop3:0x78
	v_lshlrev_b32_e32 v182, 4, v10
	v_bfe_u32 v10, v3, 2, 2
	v_lshlrev_b32_e32 v6, 2, v6
	s_add_u32 s8, s50, 0x304ae000
	v_lshrrev_b32_e32 v8, 2, v3
	v_lshrrev_b32_e32 v9, 4, v3
	v_lshlrev_b32_e32 v181, 4, v11
	v_bfe_u32 v3, v3, 4, 1
	v_or_b32_e32 v11, v6, v10
	s_addc_u32 s9, s51, 0
	v_bitop3_b32 v14, v6, v3, v10 bitop3:0x36
	v_bitop3_b32 v3, v3, v11, 4 bitop3:0x36
	s_lshr_b32 s4, s23, 31
	v_and_b32_e32 v7, 31, v0
	v_lshlrev_b32_e32 v183, 5, v14
	v_or_b32_e32 v14, 2, v9
	v_lshlrev_b32_e32 v185, 5, v3
	v_or_b32_e32 v3, 6, v9
	s_movk_i32 s3, 0x180
	s_add_i32 s4, s23, s4
	v_ashrrev_i32_e32 v2, 4, v2
	v_bitop3_b32 v14, v6, v14, v10 bitop3:0x36
	v_bitop3_b32 v3, v6, v3, v10 bitop3:0x36
	v_and_b32_e32 v9, 15, v0
	v_mad_u32_u24 v187, v7, s3, 0
	s_add_i32 s3, s23, s22
	s_ashr_i32 s4, s4, 1
	v_lshlrev_b32_e32 v10, 1, v2
	s_sub_i32 s10, s3, s4
	v_bitop3_b32 v10, v10, v9, 14 bitop3:0x6c
	v_lshlrev_b32_e32 v2, 12, v2
	s_add_u32 s12, s50, 0x2e0ae000
	v_lshl_or_b32 v168, v10, 4, v2
	v_ashrrev_i32_e32 v2, 4, v5
	s_addc_u32 s13, s51, 0
	v_lshlrev_b32_e32 v5, 1, v2
	s_add_u32 s14, s50, 0x2c48e000
	v_bitop3_b32 v5, v5, v9, 14 bitop3:0x6c
	v_lshlrev_b32_e32 v2, 12, v2
	s_addc_u32 s15, s51, 0
	v_lshl_or_b32 v170, v5, 4, v2
	v_lshl_or_b32 v189, s2, 5, v7
	s_lshl_b32 s2, s2, 10
	v_and_b32_e32 v2, 1, v4
	s_add_i32 s27, s2, 0
	v_cmp_eq_u32_e64 s[2:3], 0, v2
	v_and_b32_e32 v2, 2, v4
	s_abs_i32 s16, s23
	v_cmp_eq_u32_e64 s[4:5], 0, v2
	v_cvt_f32_u32_e32 v2, s16
	s_sub_i32 s18, 0, s16
	s_ashr_i32 s17, s10, 31
	s_abs_i32 s10, s10
	v_rcp_iflag_f32_e32 v2, v2
	v_lshlrev_b32_e32 v13, 3, v0
	v_lshlrev_b32_e32 v186, 5, v3
	v_lshrrev_b32_e32 v3, 2, v0
	v_mul_f32_e32 v2, 0x4f7ffffe, v2
	v_cvt_u32_f32_e32 v2, v2
	v_lshlrev_b32_e32 v12, 8, v11
	v_and_b32_e32 v13, 24, v13
	v_and_b32_e32 v6, 8, v3
	v_readfirstlane_b32 s19, v2
	s_mul_i32 s18, s18, s19
	s_mul_hi_u32 s18, s19, s18
	s_add_i32 s19, s19, s18
	s_mul_hi_u32 s18, s10, s19
	s_mul_i32 s18, s18, s16
	s_sub_i32 s10, s10, s18
	s_sub_i32 s18, s10, s16
	s_cmp_ge_u32 s10, s16
	s_cselect_b32 s10, s18, s10
	s_sub_i32 s18, s10, s16
	s_cmp_ge_u32 s10, s16
	s_cselect_b32 s10, s18, s10
	s_xor_b32 s10, s10, s17
	v_mov_b32_e32 v3, 0
	v_and_b32_e32 v8, 8, v8
	v_and_b32_e32 v4, 4, v4
	s_sub_i32 s34, s10, s17
	v_mbcnt_lo_u32_b32 v2, -1, 0
	v_lshlrev_b32_e32 v1, 4, v1
	v_lshlrev_b32_e32 v184, 5, v14
	s_mov_b32 s11, 0
	v_add3_u32 v188, 0, v12, v13
	v_add_u32_e32 v190, 0x400, v189
	v_mov_b32_e32 v163, v3
	v_mov_b32_e32 v165, v3
	v_cmp_eq_u32_e64 s[6:7], 0, v4
	v_mov_b32_e32 v167, v3
	v_mov_b32_e32 v169, v3
	v_mov_b32_e32 v171, v3
	s_addk_i32 s34, 0x100
	s_mov_b64 s[16:17], -1
	s_movk_i32 s35, 0xc00
	v_lshlrev_b32_e32 v172, 1, v6
	s_add_i32 s40, s27, 0x2000
	s_add_i32 s41, s27, 0x4000
	s_mov_b64 s[18:19], 0x100
	s_add_i32 s54, s27, 0x12000
	s_add_i32 s55, s27, 0x14000
	s_mov_b32 s58, 0x41000000
	v_lshlrev_b32_e32 v174, 1, v8
	v_mbcnt_hi_u32_b32 v191, -1, v2
	v_mov_b32_e32 v248, 0x2000
	v_mov_b32_e32 v249, 0x40000
	v_cndmask_b32_e64 v234, v248, v249, s[2:3]
	v_mov_b32_e32 v235, 0
	v_cndmask_b32_e64 v236, v248, v249, s[4:5]
	v_mov_b32_e32 v237, 0
	v_cndmask_b32_e64 v238, v248, v249, s[6:7]
	v_mov_b32_e32 v239, 0
	s_mov_b32 s84, 0x40000
	s_mov_b32 s85, 0
	s_branch .LBB0_546

; #define LAS __attribute__((address_space(3)))
;     DI const char* kb(int j) const { return KV + (size_t)keyrow0(j) * 4096 + head * 512; }
;     DI const char* vb(int j) const { return KV + (size_t)keyrow0(j) * 4096 + head * 512 + 256; }
;     DI const char* rb(int j) const { return KR + (size_t)keyrow0(j) * 128; }
;     DI const char* kb(int q) const { return Z + (size_t)keyrow0(q) * (L1IN * 2) + (1024 + kvh * 128) * 2; }
;     DI const char* vb(int q) const { return Z + (size_t)keyrow0(q) * (L1IN * 2) + (1280 + kvh * 128) * 2; }
;     DI const char* kb(int j) const { return Z + (size_t)keyrow0(j) * (L1IN * 2) + (2560 + head * 128) * 2; }
;     DI const char* vb(int j) const { return Z + (size_t)keyrow0(j) * (L1IN * 2) + (3584 + head * 128) * 2; }
; template <int DQ>
; DI void at_dma_k(LAS unsigned char* kslot, const char* kb, const char* rb, const AtDma& d, int wave) {
; #pragma unroll
;     for (int k = 0; k < DQ / 64; ++k) {
;         const char* src = (DQ == 192 && ((d.rope >> k) & 1u)) ? rb + d.ko[k] : kb + d.ko[k];
;         __builtin_amdgcn_global_load_lds((const unsigned*)src, (LAS unsigned*)(kslot + (wave + 8 * k) * 1024), 16, 0, 0);
;     }
; }
; DI void at_dma_v(LAS unsigned char* vslot, const char* vb, const AtDma& d, int wave) {
; #pragma unroll
;     for (int k = 0; k < 2; ++k) __builtin_amdgcn_global_load_lds((const unsigned*)(vb + d.vo[k]), (LAS unsigned*)(vslot + (wave + 8 * k) * 1024), 16, 0, 0);
; }
; template <int DQ, class Drv>
; DI void at_run3(LAS unsigned char* lds, const Drv& D, const int n, const AtRd& rd, const AtDma& dm, const bf16x8 (&qf)[DQ / 16], f32x16 (&o)[4], float& m, float& l, const float c2, const int lane, const int wave) {
;     ...
;     for (int j = 0; j < n; ++j) {
;         const int nx2 = cur == 0 ? 2 : cur - 1;
;         if (j + 2 < n) { at_dma_k<DQ>(lds + nx2 * AT4_SLOT, D.kb(j + 2), D.rb(j + 2), dm, wave); at_dma_v(lds + nx2 * AT4_SLOT + AT_KSLOT, D.vb(j + 2), dm, wave); }
.LBB0_556:
	s_mov_b32 s70, s98
	s_mov_b32 s71, s99
	s_add_i32 s98, s98, 1
	s_cmp_eq_u32 s98, 3
	s_cselect_b32 s98, 0, s98
	s_add_i32 s99, s99, 1
	s_cmp_eq_u32 s99, 3
	s_cselect_b32 s99, 0, s99
	s_add_i32 s100, s68, 2
	s_cmp_gt_u32 s100, s10
	s_cbranch_scc1 .Lmla_nodma
	s_mul_i32 s72, s71, 0x6000
	s_add_i32 s72, s27, s72
	s_lshl_b32 s71, s71, 14
	s_add_i32 s71, s27, s71
	s_cmp_eq_u32 s68, 0
	s_cbranch_scc1 .Lmla_dma_full
	s_cmp_eq_u32 s68, 2
	s_cbranch_scc1 .Lmla_dma_full
	v_lshl_add_u64 v[224:225], v[224:225], 0, v[234:235]
	v_lshl_add_u64 v[226:227], v[226:227], 0, v[236:237]
	v_lshl_add_u64 v[228:229], v[228:229], 0, v[238:239]
	v_lshl_add_u64 v[230:231], v[230:231], 0, s[84:85]
	v_lshl_add_u64 v[232:233], v[232:233], 0, s[84:85]
	s_branch .Lmla_dma_issue
.Lmla_dma_full:
	s_add_i32 s100, s69, 64
	s_cmp_lt_u32 s68, 2
	s_cselect_b64 vcc, -1, 0
	v_cndmask_b32_e32 v2, v175, v178, vcc
	v_add_u32_e32 v4, s100, v2
	v_ashrrev_i32_e32 v5, 31, v4
	v_lshlrev_b64 v[6:7], 12, v[4:5]
	v_lshlrev_b64 v[4:5], 7, v[4:5]
	v_lshl_add_u64 v[6:7], s[30:31], 0, v[6:7]
	v_lshl_add_u64 v[4:5], s[14:15], 0, v[4:5]
	v_cndmask_b32_e64 v225, v5, v7, s[2:3]
	v_cndmask_b32_e64 v224, v4, v6, s[2:3]
	v_lshl_add_u64 v[224:225], v[224:225], 0, v[162:163]
	v_cndmask_b32_e64 v227, v5, v7, s[4:5]
	v_cndmask_b32_e64 v226, v4, v6, s[4:5]
	v_lshl_add_u64 v[226:227], v[226:227], 0, v[164:165]
	v_cndmask_b32_e64 v229, v5, v7, s[6:7]
	v_cndmask_b32_e64 v228, v4, v6, s[6:7]
	v_lshl_add_u64 v[228:229], v[228:229], 0, v[166:167]
	v_lshl_add_u64 v[230:231], v[6:7], 0, v[168:169]
	v_lshl_add_u64 v[230:231], v[230:231], 0, s[18:19]
	v_lshl_add_u64 v[232:233], v[6:7], 0, v[170:171]
	v_lshl_add_u64 v[232:233], v[232:233], 0, s[18:19]
.Lmla_dma_issue:
	s_mov_b32 m0, s72
	s_nop 0
	global_load_lds_dwordx4 v[224:225], off
	s_add_i32 m0, s72, 0x2000
	s_nop 0
	global_load_lds_dwordx4 v[226:227], off
	s_add_i32 m0, s72, 0x4000
	s_nop 0
	global_load_lds_dwordx4 v[228:229], off
	s_add_i32 m0, s71, 0x12000
	s_nop 0
	global_load_lds_dwordx4 v[230:231], off
	s_add_i32 m0, s71, 0x14000
	s_nop 0
	global_load_lds_dwordx4 v[232:233], off
; #define LAS __attribute__((address_space(3)))
; #define MFMA32(a, b, c) __builtin_amdgcn_mfma_f32_32x32x16_bf16((a), (b), (c), 0, 0, 0)
;     DI NoBias bias(int) const { return NoBias(); }
;     DI WinBias bias(int q) const { const int j = tid_(q); WinBias B; B.base = j < 4 ? 100 : qpos - (k0base + 64 * (j - 4)) + 128; return B; }
; #pragma unroll
;     for (int i = 0; i < 16; ++i) { s0[i] = init; s1[i] = init; }
;     const LAS unsigned char* kp0 = ks + rd.kbase; const LAS unsigned char* kp1 = ks + rd.kbase1;
; #pragma unroll
;     for (int s = 0; s < DQ / 16; ++s) {
;         const LAS unsigned char* kp = (DQ == 128) ? ((s >> 2) ? kp1 : kp0) : kp0 + ((s >> 2) << 7);
;         const bf16x8 a0 = *(const LAS bf16x8*)(kp + rd.ko[s & 3]);
;         const bf16x8 a1 = *(const LAS bf16x8*)(kp + 32 * (DQ * 2) + rd.ko[s & 3]);
;         s0 = MFMA32(a0, qf[s], s0); s1 = MFMA32(a1, qf[s], s1);
;     }
; }
; template <class BiasFn, bool PRE = false>
; DI void at_sm(f32x16& s0, f32x16& s1, f32x16 (&o)[4], float& m, float& l, const float c2, const BiasFn& bias, const int lane, bf16x8 (&pf)[4]) {
;     const int h = lane >> 5;
;     const float nm = -m;
;     int mi = (int)0x80000000;
; #pragma unroll
;     for (int i = 0; i < 16; ++i) {
;         const int key = (i & 3) + 8 * (i >> 2) + 4 * h;
;         if (!PRE) { s0[i] = fmaf(s0[i], c2, bias(key, nm)); s1[i] = fmaf(s1[i], c2, bias(32 + key, nm)); }
;         mi = max(mi, max((int)__float_as_uint(s0[i]), (int)__float_as_uint(s1[i])));
;     }
;     { const auto sw = __builtin_amdgcn_permlane32_swap((unsigned)mi, (unsigned)mi, false, false); mi = max((int)sw[0], (int)sw[1]); }
;     const float mx = __uint_as_float((unsigned)mi);
;     if (__any(mx > 8.0f)) {
;         const float d = fmaxf(mx, 0.f), alpha = __builtin_amdgcn_exp2f(-d);
;         m += d; l *= alpha;
; #pragma unroll
;         for (int t = 0; t < 4; ++t)
; #pragma unroll
;             for (int i = 0; i < 16; ++i) o[t][i] *= alpha;
; #pragma unroll
;         for (int i = 0; i < 16; ++i) { s0[i] -= d; s1[i] -= d; }
;     }
.Lmla_nodma:
	s_mul_i32 s71, s70, 0x6000
	v_add_u32_e32 v2, s71, v187
	v_add_u32_e32 v16, v2, v1
	ds_read_b128 v[4:7], v16
	ds_read_b128 v[8:11], v16 offset:128
	v_xor_b32_e32 v82, 0x80000000, v179
	v_mov_b32_e32 v83, v82
	v_mov_b32_e32 v84, v82
	v_mov_b32_e32 v85, v82
	v_mov_b32_e32 v86, v82
	v_mov_b32_e32 v87, v82
	v_mov_b32_e32 v88, v82
	v_mov_b32_e32 v89, v82
	v_mov_b32_e32 v90, v82
	v_mov_b32_e32 v91, v82
	v_mov_b32_e32 v92, v82
	v_mov_b32_e32 v93, v82
	v_mov_b32_e32 v94, v82
	v_mov_b32_e32 v95, v82
	v_mov_b32_e32 v96, v82
	v_mov_b32_e32 v97, v82
	v_add_u32_e32 v17, v2, v180
	v_add_u32_e32 v216, v2, v181
	s_waitcnt lgkmcnt(0)
	v_mfma_f32_32x32x16_bf16 v[98:113], v[4:7], v[158:161], v[82:97]
	ds_read_b128 v[4:7], v16 offset:12288
	ds_read_b128 v[12:15], v16 offset:256
	v_add_u32_e32 v2, v2, v182
	s_waitcnt lgkmcnt(0)
	v_mfma_f32_32x32x16_bf16 v[82:97], v[4:7], v[158:161], v[82:97]
	ds_read_b128 v[4:7], v17
	ds_read_b128 v[192:195], v17 offset:128
	s_waitcnt lgkmcnt(0)
	v_mfma_f32_32x32x16_bf16 v[98:113], v[4:7], v[154:157], v[98:113]
	ds_read_b128 v[4:7], v17 offset:12288
	ds_read_b128 v[196:199], v17 offset:256
	s_waitcnt lgkmcnt(0)
	v_mfma_f32_32x32x16_bf16 v[82:97], v[4:7], v[154:157], v[82:97]
	ds_read_b128 v[4:7], v216
	ds_read_b128 v[200:203], v216 offset:128
	s_waitcnt lgkmcnt(0)
	v_mfma_f32_32x32x16_bf16 v[98:113], v[4:7], v[150:153], v[98:113]
	ds_read_b128 v[4:7], v216 offset:12288
	ds_read_b128 v[204:207], v216 offset:256
	s_waitcnt lgkmcnt(0)
	v_mfma_f32_32x32x16_bf16 v[82:97], v[4:7], v[150:153], v[82:97]
	ds_read_b128 v[4:7], v2
	ds_read_b128 v[208:211], v2 offset:128
	s_waitcnt lgkmcnt(0)
	v_mfma_f32_32x32x16_bf16 v[98:113], v[4:7], v[146:149], v[98:113]
	ds_read_b128 v[4:7], v2 offset:12288
	ds_read_b128 v[212:215], v2 offset:256
	s_waitcnt lgkmcnt(0)
	v_mfma_f32_32x32x16_bf16 v[82:97], v[4:7], v[146:149], v[82:97]
	v_mfma_f32_32x32x16_bf16 v[98:113], v[8:11], v[142:145], v[98:113]
	ds_read_b128 v[4:7], v16 offset:12416
	ds_read_b128 v[8:11], v16 offset:12544
	s_waitcnt lgkmcnt(0)
	v_mfma_f32_32x32x16_bf16 v[82:97], v[4:7], v[142:145], v[82:97]
	v_mfma_f32_32x32x16_bf16 v[98:113], v[192:195], v[138:141], v[98:113]
	ds_read_b128 v[4:7], v17 offset:12416
	ds_read_b128 v[192:195], v17 offset:12544
	s_waitcnt lgkmcnt(0)
	v_mfma_f32_32x32x16_bf16 v[82:97], v[4:7], v[138:141], v[82:97]
	v_mfma_f32_32x32x16_bf16 v[98:113], v[200:203], v[134:137], v[98:113]
	ds_read_b128 v[4:7], v216 offset:12416
	ds_read_b128 v[200:203], v216 offset:12544
	s_waitcnt lgkmcnt(0)
	v_mfma_f32_32x32x16_bf16 v[82:97], v[4:7], v[134:137], v[82:97]
	v_mfma_f32_32x32x16_bf16 v[98:113], v[208:211], v[130:133], v[98:113]
	ds_read_b128 v[4:7], v2 offset:12416
	ds_read_b128 v[208:211], v2 offset:12544
	s_waitcnt lgkmcnt(0)
	v_mfma_f32_32x32x16_bf16 v[82:97], v[4:7], v[130:133], v[82:97]
	v_mfma_f32_32x32x16_bf16 v[98:113], v[12:15], v[126:129], v[98:113]
	v_mfma_f32_32x32x16_bf16 v[82:97], v[8:11], v[126:129], v[82:97]
	v_mfma_f32_32x32x16_bf16 v[98:113], v[196:199], v[122:125], v[98:113]
	v_mfma_f32_32x32x16_bf16 v[82:97], v[192:195], v[122:125], v[82:97]
	v_mfma_f32_32x32x16_bf16 v[98:113], v[204:207], v[118:121], v[98:113]
	v_mfma_f32_32x32x16_bf16 v[82:97], v[200:203], v[118:121], v[82:97]
	v_mfma_f32_32x32x16_bf16 v[98:113], v[212:215], v[114:117], v[98:113]
	v_mfma_f32_32x32x16_bf16 v[82:97], v[208:211], v[114:117], v[82:97]
	s_nop 11
	v_max3_i32 v4, v82, v83, v84
	v_max3_i32 v5, v85, v86, v87
	v_max3_i32 v6, v88, v89, v90
	v_max3_i32 v7, v91, v92, v93
	v_max3_i32 v8, v94, v95, v96
	v_max3_i32 v9, v97, v98, v99
	v_max3_i32 v10, v100, v101, v102
	v_max3_i32 v11, v103, v104, v105
	v_max3_i32 v12, v106, v107, v108
	v_max3_i32 v13, v109, v110, v111
	v_max3_i32 v4, v4, v5, v6
	v_max3_i32 v5, v7, v8, v9
	v_max3_i32 v6, v10, v11, v12
	v_max3_i32 v7, v13, v112, v113
	v_max3_i32 v2, v4, v5, v6
	v_max_i32_e32 v2, v2, v7
	v_mov_b32_e32 v4, v2
	s_nop 1
	v_permlane32_swap_b32_e32 v2, v4
	v_max_i32_e32 v2, v2, v4
	v_cmp_lt_f32_e32 vcc, s58, v2
	s_cbranch_vccz .LBB0_555
	v_max_f32_e32 v2, v2, v2
	v_max_f32_e32 v4, 0, v2
	v_exp_f32_e64 v2, -v4
	v_add_f32_e32 v179, v179, v4
	v_sub_f32_e32 v113, v113, v4
	v_sub_f32_e32 v112, v112, v4
	v_mul_f32_e32 v173, v173, v2
	v_pk_mul_f32 v[80:81], v[80:81], v[2:3] op_sel_hi:[1,0]
	v_pk_mul_f32 v[78:79], v[78:79], v[2:3] op_sel_hi:[1,0]
	v_pk_mul_f32 v[76:77], v[76:77], v[2:3] op_sel_hi:[1,0]
	v_pk_mul_f32 v[74:75], v[74:75], v[2:3] op_sel_hi:[1,0]
	v_pk_mul_f32 v[72:73], v[72:73], v[2:3] op_sel_hi:[1,0]
	v_pk_mul_f32 v[70:71], v[70:71], v[2:3] op_sel_hi:[1,0]
	v_pk_mul_f32 v[68:69], v[68:69], v[2:3] op_sel_hi:[1,0]
	v_pk_mul_f32 v[66:67], v[66:67], v[2:3] op_sel_hi:[1,0]
	v_pk_mul_f32 v[64:65], v[64:65], v[2:3] op_sel_hi:[1,0]
	v_pk_mul_f32 v[62:63], v[62:63], v[2:3] op_sel_hi:[1,0]
	v_pk_mul_f32 v[60:61], v[60:61], v[2:3] op_sel_hi:[1,0]
	v_pk_mul_f32 v[58:59], v[58:59], v[2:3] op_sel_hi:[1,0]
	v_pk_mul_f32 v[56:57], v[56:57], v[2:3] op_sel_hi:[1,0]
	v_pk_mul_f32 v[54:55], v[54:55], v[2:3] op_sel_hi:[1,0]
	v_pk_mul_f32 v[52:53], v[52:53], v[2:3] op_sel_hi:[1,0]
	v_pk_mul_f32 v[50:51], v[50:51], v[2:3] op_sel_hi:[1,0]
	v_pk_mul_f32 v[48:49], v[48:49], v[2:3] op_sel_hi:[1,0]
	v_pk_mul_f32 v[46:47], v[46:47], v[2:3] op_sel_hi:[1,0]
	v_pk_mul_f32 v[44:45], v[44:45], v[2:3] op_sel_hi:[1,0]
	v_pk_mul_f32 v[42:43], v[42:43], v[2:3] op_sel_hi:[1,0]
	v_pk_mul_f32 v[40:41], v[40:41], v[2:3] op_sel_hi:[1,0]
	v_pk_mul_f32 v[38:39], v[38:39], v[2:3] op_sel_hi:[1,0]
	v_pk_mul_f32 v[36:37], v[36:37], v[2:3] op_sel_hi:[1,0]
	v_pk_mul_f32 v[34:35], v[34:35], v[2:3] op_sel_hi:[1,0]
	v_pk_mul_f32 v[32:33], v[32:33], v[2:3] op_sel_hi:[1,0]
	v_pk_mul_f32 v[30:31], v[30:31], v[2:3] op_sel_hi:[1,0]
	v_pk_mul_f32 v[28:29], v[28:29], v[2:3] op_sel_hi:[1,0]
	v_pk_mul_f32 v[26:27], v[26:27], v[2:3] op_sel_hi:[1,0]
	v_pk_mul_f32 v[24:25], v[24:25], v[2:3] op_sel_hi:[1,0]
	v_pk_mul_f32 v[22:23], v[22:23], v[2:3] op_sel_hi:[1,0]
	v_pk_mul_f32 v[20:21], v[20:21], v[2:3] op_sel_hi:[1,0]
	v_pk_mul_f32 v[18:19], v[18:19], v[2:3] op_sel_hi:[1,0]
	v_sub_f32_e32 v111, v111, v4
	v_sub_f32_e32 v110, v110, v4
	v_sub_f32_e32 v109, v109, v4
	v_sub_f32_e32 v108, v108, v4
	v_sub_f32_e32 v107, v107, v4
	v_sub_f32_e32 v106, v106, v4
	v_sub_f32_e32 v105, v105, v4
	v_sub_f32_e32 v104, v104, v4
	v_sub_f32_e32 v103, v103, v4
	v_sub_f32_e32 v102, v102, v4
	v_sub_f32_e32 v101, v101, v4
	v_sub_f32_e32 v100, v100, v4
	v_sub_f32_e32 v99, v99, v4
	v_sub_f32_e32 v98, v98, v4
	v_sub_f32_e32 v97, v97, v4
	v_sub_f32_e32 v96, v96, v4
	v_sub_f32_e32 v95, v95, v4
	v_sub_f32_e32 v94, v94, v4
	v_sub_f32_e32 v93, v93, v4
	v_sub_f32_e32 v92, v92, v4
	v_sub_f32_e32 v91, v91, v4
	v_sub_f32_e32 v90, v90, v4
	v_sub_f32_e32 v89, v89, v4
	v_sub_f32_e32 v88, v88, v4
	v_sub_f32_e32 v87, v87, v4
	v_sub_f32_e32 v86, v86, v4
	v_sub_f32_e32 v85, v85, v4
	v_sub_f32_e32 v84, v84, v4
	v_sub_f32_e32 v83, v83, v4
	v_sub_f32_e32 v82, v82, v4
	s_branch .LBB0_555
